# v28: v27 + the remaining pixel-index v_mul_lo_u32 (k_point store address x72, nca1 heads x7) as full-rate v_mul_u32_u24 (bit-exact)
# speedup vs baseline: 1.0220x; 1.0037x over previous
.LBB0_24:
	s_or_b64 exec, exec, s[0:1]
	s_waitcnt vmcnt(0)
	v_pk_mul_f32 v[124:125], v[54:55], 0.5 op_sel_hi:[1,0]
	v_pk_mul_f32 v[138:139], v[56:57], 0.5 op_sel_hi:[1,0]
	v_and_b32_e32 v126, 0x7fffffff, v124
	v_and_b32_e32 v140, 0x7fffffff, v138
	v_and_b32_e32 v127, 0x7fffffff, v125
	v_and_b32_e32 v141, 0x7fffffff, v139
	v_pk_mul_f32 v[128:129], v[126:127], s[24:25] op_sel_hi:[1,0]
	v_pk_mul_f32 v[142:143], v[140:141], s[24:25] op_sel_hi:[1,0]
	v_pk_fma_f32 v[130:131], v[128:129], s[26:27], 1.0 op_sel_hi:[1,0,0]
	v_pk_fma_f32 v[144:145], v[142:143], s[26:27], 1.0 op_sel_hi:[1,0,0]
	v_pk_mul_f32 v[132:133], v[128:129], s[28:29] op_sel_hi:[1,0]
	v_pk_mul_f32 v[146:147], v[142:143], s[28:29] op_sel_hi:[1,0]
	v_rcp_f32_e32 v130, v130
	v_rcp_f32_e32 v144, v144
	v_rcp_f32_e32 v131, v131
	v_rcp_f32_e32 v145, v145
	v_pk_mul_f32 v[132:133], v[128:129], v[132:133]
	v_pk_mul_f32 v[146:147], v[142:143], v[146:147]
	v_exp_f32_e32 v132, v132
	v_exp_f32_e32 v146, v146
	v_exp_f32_e32 v133, v133
	v_exp_f32_e32 v147, v147
	v_pk_fma_f32 v[134:135], v[130:131], s[30:31], v[152:153] op_sel_hi:[1,0,0]
	v_pk_fma_f32 v[148:149], v[144:145], s[30:31], v[152:153] op_sel_hi:[1,0,0]
	v_pk_fma_f32 v[134:135], v[134:135], v[130:131], s[34:35] op_sel_hi:[1,1,0]
	v_pk_fma_f32 v[148:149], v[148:149], v[144:145], s[34:35] op_sel_hi:[1,1,0]
	v_pk_fma_f32 v[134:135], v[134:135], v[130:131], s[36:37] op_sel_hi:[1,1,0]
	v_pk_fma_f32 v[148:149], v[148:149], v[144:145], s[36:37] op_sel_hi:[1,1,0]
	v_pk_fma_f32 v[134:135], v[134:135], v[130:131], s[38:39] op_sel_hi:[1,1,0]
	v_pk_fma_f32 v[148:149], v[148:149], v[144:145], s[38:39] op_sel_hi:[1,1,0]
	v_pk_mul_f32 v[134:135], v[130:131], v[134:135]
	v_pk_mul_f32 v[148:149], v[144:145], v[148:149]
	v_pk_mul_f32 v[134:135], v[132:133], v[134:135]
	v_pk_mul_f32 v[148:149], v[146:147], v[148:149]
	v_pk_fma_f32 v[136:137], v[54:55], 0.5, v[126:127] op_sel_hi:[1,0,1]
	v_pk_fma_f32 v[150:151], v[56:57], 0.5, v[140:141] op_sel_hi:[1,0,1]
	v_pk_fma_f32 v[82:83], v[126:127], v[134:135], v[136:137] neg_lo:[1,0,0] neg_hi:[1,0,0]
	v_pk_fma_f32 v[84:85], v[140:141], v[148:149], v[150:151] neg_lo:[1,0,0] neg_hi:[1,0,0]
	v_cvt_pk_f16_f32 v73, v60, v61
	v_cvt_pk_f16_f32 v71, v80, v81
	v_cvt_pk_f16_f32 v70, v78, v79
	v_cvt_pk_f16_f32 v72, v58, v59
	v_cvt_pk_f16_f32 v69, v76, v77
	v_lshlrev_b32_e32 v50, 1, v93
	v_cvt_pk_f16_f32 v67, v64, v65
	v_cvt_pk_f16_f32 v66, v62, v63
	v_cvt_pk_f16_f32 v68, v74, v75
	s_and_saveexec_b64 s[6:7], s[4:5]
	s_xor_b64 s[6:7], exec, s[6:7]
	s_cbranch_execz .LBB0_14
	s_movk_i32 s10, 0x48
	v_mul_u32_u24_e32 v0, s10, v97
	v_ashrrev_i32_e32 v1, 31, v0
	v_mov_b32_e32 v51, v52
	s_waitcnt lgkmcnt(0)
	v_lshl_add_u64 v[0:1], v[0:1], 1, s[64:65]
	v_lshl_add_u64 v[0:1], v[0:1], 0, v[50:51]
	v_cvt_pk_f16_f32 v55, v64, v65
	v_cvt_pk_f16_f32 v54, v62, v63
	global_store_dwordx2 v[0:1], v[54:55], off
	v_cvt_pk_f16_f32 v55, v76, v77
	v_cvt_pk_f16_f32 v54, v74, v75
	global_store_dwordx2 v[0:1], v[54:55], off offset:32
	v_cvt_pk_f16_f32 v55, v80, v81
	v_cvt_pk_f16_f32 v54, v78, v79
	v_cmp_gt_u32_e64 s[4:5], 32, v103
	global_store_dwordx2 v[0:1], v[54:55], off offset:64
	v_cvt_pk_f16_f32 v55, v60, v61
	v_cvt_pk_f16_f32 v54, v58, v59
	global_store_dwordx2 v[0:1], v[54:55], off offset:96
	s_and_saveexec_b64 s[8:9], s[4:5]
	s_cbranch_execz .LBB0_13
	v_cvt_pk_f16_f32 v55, v84, v85
	v_cvt_pk_f16_f32 v54, v82, v83
	global_store_dwordx2 v[0:1], v[54:55], off offset:128

.LBB0_26:
	s_or_b64 exec, exec, s[2:3]
	v_or_b32_e32 v0, 2, v104
	s_movk_i32 s0, 0x2d00
	v_mad_u32_u24 v28, v0, s0, 0
	v_mul_u32_u24_e32 v0, 0x140, v0
	v_lshlrev_b32_e32 v1, 2, v93
	v_add_u32_e32 v30, v28, v88
	v_add3_u32 v29, s11, v0, v1
	v_add3_u32 v32, v28, v92, v88
	v_add_u32_e32 v33, v30, v92
	ds_read_b128 v[0:3], v29
	ds_read_b64_tr_b16 v[4:5], v32
	ds_read_b64_tr_b16 v[6:7], v33 offset:2560
	v_mov_b32_e32 v62, v52
	ds_read_b64_tr_b16 v[8:9], v32 offset:32
	v_lshl_add_u32 v31, v91, 1, v28
	s_waitcnt lgkmcnt(1)
	v_mfma_f32_16x16x32_f16 v[4:7], v[4:7], v[62:65], v[0:3]
	ds_read_b64_tr_b16 v[10:11], v33 offset:2592
	ds_read_b64_tr_b16 v[12:13], v32 offset:5120
	ds_read_b64_tr_b16 v[14:15], v33 offset:7680
	v_add_u32_e32 v34, v31, v92
	ds_read_b64_tr_b16 v[0:1], v34 offset:10240
	v_mov_b32_e32 v2, 0
	v_mov_b32_e32 v3, v2
	s_waitcnt lgkmcnt(1)
	v_mfma_f32_16x16x32_f16 v[4:7], v[12:15], v[58:61], v[4:7]
	ds_read_b64_tr_b16 v[12:13], v34 offset:10272
	ds_read_b128 v[16:19], v29 offset:64
	v_mov_b32_e32 v14, v2
	s_waitcnt lgkmcnt(2)
	v_mfma_f32_16x16x32_f16 v[4:7], v[0:3], v[54:57], v[4:7]
	ds_read_b64_tr_b16 v[20:21], v32 offset:5152
	ds_read_b64_tr_b16 v[22:23], v33 offset:7712
	v_mov_b32_e32 v15, v2
	s_waitcnt lgkmcnt(2)
	v_mfma_f32_16x16x32_f16 v[8:11], v[8:11], v[62:65], v[16:19]
	ds_read_b64_tr_b16 v[24:25], v32 offset:64
	v_add3_u32 v28, v28, v95, v88
	v_add_u32_e32 v30, v30, v95
	ds_read_b128 v[16:19], v29 offset:128
	s_waitcnt lgkmcnt(2)
	v_mfma_f32_16x16x32_f16 v[8:11], v[20:23], v[58:61], v[8:11]
	ds_read_b64_tr_b16 v[26:27], v33 offset:2624
	ds_read_b64_tr_b16 v[20:21], v32 offset:5184
	s_movk_i32 s2, 0x90
	v_mfma_f32_16x16x32_f16 v[8:11], v[12:15], v[54:57], v[8:11]
	ds_read_b64_tr_b16 v[22:23], v33 offset:7744
	ds_read_b64_tr_b16 v[0:1], v34 offset:10304
	v_mad_u32_u24 v35, v102, s2, v86
	s_waitcnt lgkmcnt(3)
	v_mfma_f32_16x16x32_f16 v[12:15], v[24:27], v[62:65], v[16:19]
	ds_read_b64_tr_b16 v[24:25], v28
	s_nop 1
	ds_read_b128 v[16:19], v29 offset:192
	v_add_u32_e32 v49, v35, v50
	s_waitcnt lgkmcnt(3)
	v_mfma_f32_16x16x32_f16 v[12:15], v[20:23], v[58:61], v[12:15]
	ds_read_b64_tr_b16 v[26:27], v30 offset:2560
	ds_read_b64_tr_b16 v[20:21], v28 offset:5120
	v_lshlrev_b32_e32 v48, 1, v87
	s_waitcnt lgkmcnt(4)
	v_mfma_f32_16x16x32_f16 v[12:15], v[0:3], v[54:57], v[12:15]
	ds_read_b64_tr_b16 v[22:23], v30 offset:7680
	v_add_u32_e32 v0, v31, v95
	ds_read_b64_tr_b16 v[0:1], v0 offset:10240
	s_waitcnt lgkmcnt(3)
	v_mfma_f32_16x16x32_f16 v[16:19], v[24:27], v[62:65], v[16:19]
	ds_read_b128 v[24:27], v29 offset:256
	ds_read_b64_tr_b16 v[28:29], v32 offset:128
	v_add_u32_e32 v36, v35, v48
	s_waitcnt lgkmcnt(3)
	v_mfma_f32_16x16x32_f16 v[16:19], v[20:23], v[58:61], v[16:19]
	ds_read_b64_tr_b16 v[30:31], v33 offset:2688
	ds_read_b64_tr_b16 v[20:21], v32 offset:5248
	v_add_u32_e32 v32, 0xb000, v49
	s_waitcnt lgkmcnt(4)
	v_mfma_f32_16x16x32_f16 v[16:19], v[0:3], v[54:57], v[16:19]
	ds_read_b64_tr_b16 v[22:23], v33 offset:7808
	ds_read_b64_tr_b16 v[0:1], v34 offset:10368
	v_add_u32_e32 v44, 0x80, v36
	v_add_u32_e32 v134, 0x180, v36
	s_waitcnt lgkmcnt(3)
	v_mfma_f32_16x16x32_f16 v[24:27], v[28:31], v[62:65], v[24:27]
	ds_read2_b64 v[28:31], v32 offset0:128 offset1:132
	ds_read2_b64 v[32:35], v32 offset0:136 offset1:140
	v_add_u32_e32 v40, 0xb800, v49
	s_waitcnt lgkmcnt(3)
	v_mfma_f32_16x16x32_f16 v[20:23], v[20:23], v[58:61], v[24:27]
	ds_read2_b64 v[36:39], v40 offset0:160 offset1:164
	v_cmp_gt_u32_e64 s[0:1], 32, v103
	v_cvt_pk_f16_f32 v11, v10, v11
	ds_read2st64_b64 v[126:129], v44 offset0:90 offset1:99
	s_waitcnt lgkmcnt(4)
	v_mfma_f32_16x16x32_f16 v[20:23], v[0:3], v[54:57], v[20:23]
	v_cvt_pk_f16_f32 v10, v8, v9
	v_cvt_pk_f16_f32 v9, v6, v7
	v_cvt_pk_f16_f32 v8, v4, v5
	ds_read2_b64 v[4:7], v40 offset0:168 offset1:172
	v_cvt_pk_f16_f32 v19, v18, v19
	s_nop 2
	v_cvt_pk_f16_f32 v0, v22, v23
	v_cvt_pk_f16_f32 v1, v20, v21
	v_cndmask_b32_e64 v21, 0, v0, s[0:1]
	v_add_u32_e32 v0, 0xc600, v49
	ds_read2_b64 v[40:43], v0 offset1:4
	s_waitcnt lgkmcnt(5)
	v_mfma_f32_16x16x32_f16 v[28:31], v[28:31], v[8:11], 0
	v_cndmask_b32_e64 v20, 0, v1, s[0:1]
	v_cvt_pk_f16_f32 v18, v16, v17
	v_cvt_pk_f16_f32 v17, v14, v15
	v_cvt_pk_f16_f32 v16, v12, v13
	ds_read2_b64 v[12:15], v0 offset0:8 offset1:12
	s_waitcnt lgkmcnt(3)
	v_mov_b32_e32 v0, v126
	v_mov_b32_e32 v1, v127
	ds_read2st64_b64 v[130:133], v134 offset0:94 offset1:103
	v_mfma_f32_16x16x32_f16 v[28:31], v[32:35], v[16:19], v[28:31]
	v_mov_b32_e32 v22, v2
	v_mov_b32_e32 v23, v2
	v_add_u32_e32 v24, 0xce00, v49
	ds_read2_b64 v[32:35], v24 offset0:32 offset1:36
	ds_read2_b64 v[52:55], v24 offset0:40 offset1:44
	v_mfma_f32_16x16x32_f16 v[28:31], v[0:3], v[20:23], v[28:31]
	v_or_b32_e32 v0, 64, v102
	v_min_u32_e32 v0, 0x47, v0
	v_mad_u32_u24 v49, v0, s2, v86
	v_add_u32_e32 v0, v49, v50
	v_add_u32_e32 v0, 0xb000, v0
	ds_read2_b64 v[56:59], v0 offset0:128 offset1:132
	ds_read2_b64 v[60:63], v0 offset0:136 offset1:140
	v_mfma_f32_16x16x32_f16 v[36:39], v[36:39], v[8:11], 0
	s_waitcnt lgkmcnt(4)
	v_mov_b32_e32 v0, v130
	v_mov_b32_e32 v1, v131
	s_movk_i32 s2, 0x48
	s_waitcnt lgkmcnt(7)
	v_mfma_f32_16x16x32_f16 v[4:7], v[4:7], v[16:19], v[36:39]
	v_mov_b32_e32 v51, v2
	v_mfma_f32_16x16x32_f16 v[24:27], v[0:3], v[20:23], v[4:7]
	s_waitcnt lgkmcnt(4)
	v_mov_b32_e32 v0, v128
	v_mov_b32_e32 v1, v129
	v_mfma_f32_16x16x32_f16 v[4:7], v[40:43], v[8:11], 0
	v_mfma_f32_16x16x32_f16 v[4:7], v[12:15], v[16:19], v[4:7]
	v_mfma_f32_16x16x32_f16 v[12:15], v[0:3], v[20:23], v[4:7]
	v_mov_b32_e32 v0, v132
	v_mov_b32_e32 v1, v133
	s_waitcnt lgkmcnt(3)
	v_mfma_f32_16x16x32_f16 v[4:7], v[32:35], v[8:11], 0
	s_waitcnt lgkmcnt(2)
	v_mfma_f32_16x16x32_f16 v[4:7], v[52:55], v[16:19], v[4:7]
	v_mfma_f32_16x16x32_f16 v[32:35], v[0:3], v[20:23], v[4:7]
	v_add_u32_e32 v0, v49, v48
	ds_read_b64 v[0:1], v0 offset:46208
	s_waitcnt lgkmcnt(2)
	v_mfma_f32_16x16x32_f16 v[4:7], v[56:59], v[8:11], 0
	v_mul_u32_u24_e32 v8, s2, v97
	s_mov_b32 s2, 0x3e2e1a92
	v_ashrrev_i32_e32 v9, 31, v8
	s_waitcnt lgkmcnt(1)
	v_mfma_f32_16x16x32_f16 v[4:7], v[60:63], v[16:19], v[4:7]
	s_waitcnt lgkmcnt(0)
	v_mfma_f32_16x16x32_f16 v[4:7], v[0:3], v[20:23], v[4:7]
	v_mov_b32_e32 v0, s63
	v_mov_b32_e32 v1, s61
	v_cndmask_b32_e32 v1, v0, v1, vcc
	v_mov_b32_e32 v0, s62
	v_mov_b32_e32 v3, s60
	v_cndmask_b32_e32 v0, v0, v3, vcc
	v_mov_b32_e32 v2, v29
	v_mov_b32_e32 v3, v30
	v_pk_mul_f32 v[2:3], v[2:3], s[2:3] op_sel_hi:[1,0]
	v_lshl_add_u64 v[0:1], v[8:9], 1, v[0:1]
	v_fma_mixlo_f16 v8, v28, s2, 0
	v_cvt_pk_f16_f32 v3, v2, v3
	v_pack_b32_f16 v2, v8, v3
	v_fma_mixlo_f16 v8, v31, s2, 0
	v_lshl_add_u64 v[0:1], v[0:1], 0, v[50:51]
	v_alignbit_b32 v3, v8, v3, 16
	global_store_dwordx2 v[0:1], v[2:3], off
	v_mov_b32_e32 v2, v25
	v_mov_b32_e32 v3, v26
	v_pk_mul_f32 v[2:3], v[2:3], s[2:3] op_sel_hi:[1,0]
	v_fma_mixlo_f16 v8, v24, s2, 0
	v_cvt_pk_f16_f32 v3, v2, v3
	v_pack_b32_f16 v2, v8, v3
	v_fma_mixlo_f16 v8, v27, s2, 0
	v_alignbit_b32 v3, v8, v3, 16
	global_store_dwordx2 v[0:1], v[2:3], off offset:32
	v_mov_b32_e32 v2, v13
	v_mov_b32_e32 v3, v14
	v_pk_mul_f32 v[2:3], v[2:3], s[2:3] op_sel_hi:[1,0]
	v_fma_mixlo_f16 v8, v12, s2, 0
	v_cvt_pk_f16_f32 v3, v2, v3
	v_pack_b32_f16 v2, v8, v3
	v_fma_mixlo_f16 v8, v15, s2, 0
	v_alignbit_b32 v3, v8, v3, 16
	global_store_dwordx2 v[0:1], v[2:3], off offset:64
	v_mov_b32_e32 v2, v33
	v_mov_b32_e32 v3, v34
	v_pk_mul_f32 v[2:3], v[2:3], s[2:3] op_sel_hi:[1,0]
	v_fma_mixlo_f16 v8, v32, s2, 0
	v_cvt_pk_f16_f32 v3, v2, v3
	v_pack_b32_f16 v2, v8, v3
	v_fma_mixlo_f16 v8, v35, s2, 0
	v_alignbit_b32 v3, v8, v3, 16
	global_store_dwordx2 v[0:1], v[2:3], off offset:96
	s_and_saveexec_b64 s[4:5], s[0:1]
	s_cbranch_execz .LBB0_28
	v_mov_b32_e32 v2, v5
	v_mov_b32_e32 v3, v6
	v_pk_mul_f32 v[2:3], v[2:3], s[2:3] op_sel_hi:[1,0]
	v_fma_mixlo_f16 v4, v4, s2, 0
	v_cvt_pk_f16_f32 v3, v2, v3
	v_pack_b32_f16 v2, v4, v3
	v_fma_mixlo_f16 v4, v7, s2, 0
	v_alignbit_b32 v3, v4, v3, 16
	global_store_dwordx2 v[0:1], v[2:3], off offset:128

.LBB2_26:
	s_or_b64 exec, exec, s[0:1]
	s_add_i32 s0, 0, 0x11880
	s_movk_i32 s1, 0x1600
	v_mov_b32_e32 v6, s0
	v_mad_u32_u24 v7, v26, s1, v6
	v_lshlrev_b32_e32 v8, 2, v38
	v_add_u32_e32 v9, v7, v8
	ds_write2st64_b32 v9, v22, v23 offset1:1
	ds_write2st64_b32 v9, v24, v25 offset0:2 offset1:3
	ds_write2st64_b32 v9, v18, v19 offset0:4 offset1:5
	ds_write2st64_b32 v9, v20, v21 offset0:6 offset1:7
	ds_write2st64_b32 v9, v14, v15 offset0:8 offset1:9
	ds_write2st64_b32 v9, v16, v17 offset0:10 offset1:11
	ds_write2st64_b32 v9, v10, v11 offset0:12 offset1:13
	ds_write2st64_b32 v9, v12, v13 offset0:14 offset1:15
	ds_write2st64_b32 v9, v2, v3 offset0:16 offset1:17
	ds_write2st64_b32 v9, v4, v5 offset0:18 offset1:19
	ds_write_b32 v9, v28 offset:5120
	v_xor_b32_e32 v9, 4, v26
	v_mad_u32_u24 v6, v9, s1, v6
	v_add_u32_e32 v29, v6, v8
	s_waitcnt lgkmcnt(0)
	s_barrier
	ds_read_b32 v8, v29 offset:5120
	v_lshlrev_b32_e32 v27, 2, v59
	v_add_u32_e32 v7, v7, v27
	v_add_u32_e32 v6, v6, v27
	ds_read_b32 v141, v6 offset:4224
	ds_read_b32 v140, v7 offset:4224
	ds_read2st64_b32 v[36:37], v29 offset0:18 offset1:19
	ds_read2st64_b32 v[30:31], v29 offset0:16 offset1:17
	ds_read2st64_b32 v[32:33], v29 offset1:1
	ds_read2st64_b32 v[34:35], v29 offset0:2 offset1:3
	ds_read2st64_b32 v[40:41], v29 offset0:4 offset1:5
	ds_read2st64_b32 v[42:43], v29 offset0:6 offset1:7
	ds_read2st64_b32 v[48:49], v29 offset0:8 offset1:9
	ds_read2st64_b32 v[52:53], v29 offset0:10 offset1:11
	ds_read2st64_b32 v[54:55], v29 offset0:12 offset1:13
	ds_read2st64_b32 v[62:63], v29 offset0:14 offset1:15
	s_waitcnt lgkmcnt(12)
	v_max_f32_e32 v6, v8, v8
	v_max_f32_e32 v7, v28, v28
	v_max_f32_e32 v6, v7, v6
	v_sub_f32_e32 v7, v28, v6
	v_sub_f32_e32 v6, v8, v6
	v_exp_f32_e32 v142, v7
	v_exp_f32_e32 v143, v6
	v_lshl_add_u32 v28, v39, 2, 0
	v_add_u32_e32 v51, 0x10e00, v28
	ds_read_b128 v[6:9], v51
	s_waitcnt lgkmcnt(11)
	v_pk_mul_f32 v[140:141], v[140:141], v[142:143]
	s_nop 0
	v_add_f32_e32 v144, v140, v141
	v_rcp_f32_e32 v144, v144
	s_movk_i32 s0, 0xa0
	s_nop 0
	v_mul_f32_e32 v44, v142, v144
	v_mul_f32_e32 v46, v143, v144
	s_waitcnt lgkmcnt(8)
	v_pk_mul_f32 v[32:33], v[46:47], v[32:33] op_sel_hi:[0,1]
	v_pk_fma_f32 v[22:23], v[44:45], v[22:23], v[32:33] op_sel_hi:[0,1,1]
	v_cvt_pk_f16_f32 v32, v22, v23
	s_waitcnt lgkmcnt(7)
	v_pk_mul_f32 v[22:23], v[46:47], v[34:35] op_sel_hi:[0,1]
	v_pk_fma_f32 v[22:23], v[44:45], v[24:25], v[22:23] op_sel_hi:[0,1,1]
	v_cvt_pk_f16_f32 v33, v22, v23
	s_waitcnt lgkmcnt(6)
	v_pk_mul_f32 v[22:23], v[46:47], v[40:41] op_sel_hi:[0,1]
	v_pk_fma_f32 v[18:19], v[44:45], v[18:19], v[22:23] op_sel_hi:[0,1,1]
	v_cvt_pk_f16_f32 v34, v18, v19
	s_waitcnt lgkmcnt(5)
	v_pk_mul_f32 v[18:19], v[46:47], v[42:43] op_sel_hi:[0,1]
	v_pk_fma_f32 v[18:19], v[44:45], v[20:21], v[18:19] op_sel_hi:[0,1,1]
	v_cvt_pk_f16_f32 v35, v18, v19
	s_waitcnt lgkmcnt(4)
	v_pk_mul_f32 v[18:19], v[46:47], v[48:49] op_sel_hi:[0,1]
	v_pk_fma_f32 v[14:15], v[44:45], v[14:15], v[18:19] op_sel_hi:[0,1,1]
	v_cvt_pk_f16_f32 v40, v14, v15
	s_waitcnt lgkmcnt(3)
	v_pk_mul_f32 v[14:15], v[46:47], v[52:53] op_sel_hi:[0,1]
	v_pk_fma_f32 v[14:15], v[44:45], v[16:17], v[14:15] op_sel_hi:[0,1,1]
	v_cvt_pk_f16_f32 v41, v14, v15
	s_waitcnt lgkmcnt(2)
	v_pk_mul_f32 v[14:15], v[46:47], v[54:55] op_sel_hi:[0,1]
	v_pk_fma_f32 v[10:11], v[44:45], v[10:11], v[14:15] op_sel_hi:[0,1,1]
	v_cvt_pk_f16_f32 v42, v10, v11
	s_waitcnt lgkmcnt(0)
	v_pk_mul_f32 v[10:11], v[46:47], v[62:63] op_sel_hi:[0,1]
	v_pk_fma_f32 v[10:11], v[44:45], v[12:13], v[10:11] op_sel_hi:[0,1,1]
	v_cvt_pk_f16_f32 v43, v10, v11
	v_pk_mul_f32 v[10:11], v[46:47], v[30:31] op_sel_hi:[0,1]
	v_pk_fma_f32 v[2:3], v[44:45], v[2:3], v[10:11] op_sel_hi:[0,1,1]
	v_cvt_pk_f16_f32 v24, v2, v3
	v_pk_mul_f32 v[2:3], v[46:47], v[36:37] op_sel_hi:[0,1]
	v_pk_fma_f32 v[2:3], v[44:45], v[4:5], v[2:3] op_sel_hi:[0,1,1]
	v_or_b32_e32 v30, v39, v60
	v_cvt_pk_f16_f32 v2, v2, v3
	v_cmp_lt_u32_e32 vcc, 31, v38
	v_and_or_b32 v29, v39, 4, v60
	v_mul_u32_u24_e32 v3, 0x50, v30
	v_cndmask_b32_e64 v45, v2, 0, vcc
	v_mad_u32_u24 v2, v29, s0, 0
	v_lshlrev_b32_e32 v36, 3, v59
	v_lshlrev_b32_e32 v48, 1, v3
	v_add_u32_e32 v31, 0xe100, v2
	v_and_b32_e32 v2, 24, v36
	v_add_u32_e32 v49, 0, v48
	v_add_u32_e32 v44, v49, v2
	v_add_u32_e32 v37, v31, v2
	v_add3_u32 v25, 0, v2, v48
	ds_read_b64_tr_b16 v[12:13], v44 offset:60160
	ds_read_b64_tr_b16 v[10:11], v25 offset:57600
	ds_read_b64_tr_b16 v[14:15], v25 offset:62720
	ds_read_b64_tr_b16 v[16:17], v44 offset:65280
	ds_read_b64_tr_b16 v[2:3], v37 offset:10240
	ds_read_b64_tr_b16 v[18:19], v25 offset:57664
	ds_read_b64_tr_b16 v[22:23], v37 offset:10272
	ds_read_b64_tr_b16 v[54:55], v44 offset:60192
	ds_read_b64_tr_b16 v[20:21], v44 offset:60224
	ds_read_b64_tr_b16 v[62:63], v44 offset:60288
	s_waitcnt lgkmcnt(8)
	v_mfma_f32_16x16x32_f16 v[6:9], v[10:13], v[32:35], v[6:9]
	v_mov_b32_e32 v4, 0
	v_mov_b32_e32 v5, v4
	ds_read_b64_tr_b16 v[52:53], v25 offset:57632
	ds_read_b64_tr_b16 v[10:11], v25 offset:62784
	s_waitcnt vmcnt(1)
	ds_read_b64_tr_b16 v[66:67], v44 offset:65312
	ds_read_b64_tr_b16 v[12:13], v44 offset:65344
	ds_read_b64_tr_b16 v[70:71], v44 offset:65408
	s_waitcnt lgkmcnt(11)
	v_mfma_f32_16x16x32_f16 v[6:9], v[14:17], v[40:43], v[6:9]
	v_cndmask_b32_e64 v44, v24, 0, vcc
	v_mov_b32_e32 v46, v4
	v_mov_b32_e32 v47, v4
	v_mov_b32_e32 v24, v4
	v_or_b32_e32 v36, 0x60, v36
	s_waitcnt lgkmcnt(10)
	v_mfma_f32_16x16x32_f16 v[14:17], v[2:5], v[44:47], v[6:9]
	s_nop 2
	ds_read_b128 v[6:9], v51 offset:64
	s_waitcnt vmcnt(0)
	ds_read_b128 v[72:75], v51 offset:128
	ds_read_b64_tr_b16 v[2:3], v37 offset:10304
	ds_read_b64_tr_b16 v[64:65], v25 offset:62752
	ds_read_b64_tr_b16 v[68:69], v25 offset:62848
	ds_read_b64_tr_b16 v[60:61], v25 offset:57728
	v_mov_b32_e32 v25, v4
	s_waitcnt lgkmcnt(5)
	v_mfma_f32_16x16x32_f16 v[6:9], v[52:55], v[32:35], v[6:9]
	v_add3_u32 v48, 0, v36, v48
	v_add_u32_e32 v49, v49, v36
	s_movk_i32 s0, 0xff
	s_waitcnt lgkmcnt(2)
	v_mfma_f32_16x16x32_f16 v[6:9], v[64:67], v[40:43], v[6:9]
	v_cmp_lt_u32_e64 s[0:1], s0, v0
	v_mfma_f32_16x16x32_f16 v[22:25], v[22:25], v[44:47], v[6:9]
	v_mfma_f32_16x16x32_f16 v[6:9], v[18:21], v[32:35], v[72:75]
	ds_read_b64_tr_b16 v[18:19], v48 offset:57600
	ds_read_b64_tr_b16 v[20:21], v49 offset:60160
	v_mfma_f32_16x16x32_f16 v[6:9], v[10:13], v[40:43], v[6:9]
	v_mfma_f32_16x16x32_f16 v[10:13], v[2:5], v[44:47], v[6:9]
	v_add_u32_e32 v2, v31, v36
	s_nop 5
	ds_read_b128 v[6:9], v51 offset:192
	ds_read_b64_tr_b16 v[52:53], v48 offset:62720
	ds_read_b64_tr_b16 v[2:3], v2 offset:10240
	ds_read_b128 v[64:67], v51 offset:256
	ds_read_b64_tr_b16 v[54:55], v49 offset:65280
	s_waitcnt lgkmcnt(4)
	v_mfma_f32_16x16x32_f16 v[6:9], v[18:21], v[32:35], v[6:9]
	s_waitcnt lgkmcnt(0)
	v_mfma_f32_16x16x32_f16 v[6:9], v[52:55], v[40:43], v[6:9]
	v_mfma_f32_16x16x32_f16 v[18:21], v[2:5], v[44:47], v[6:9]
	ds_read_b64_tr_b16 v[2:3], v37 offset:10368
	v_mfma_f32_16x16x32_f16 v[6:9], v[60:63], v[32:35], v[64:67]
	v_mfma_f32_16x16x32_f16 v[6:9], v[68:71], v[40:43], v[6:9]
	s_waitcnt lgkmcnt(0)
	v_mfma_f32_16x16x32_f16 v[6:9], v[2:5], v[44:47], v[6:9]
	s_and_saveexec_b64 s[6:7], s[0:1]
	s_xor_b64 s[0:1], exec, s[6:7]
	s_cbranch_execz .LBB2_38
	v_lshlrev_b32_e32 v5, 2, v1
	s_add_i32 s6, 0, 0x10f40
	v_cvt_pk_f16_f32 v0, v14, v15
	v_add_u32_e32 v14, 0x11840, v28
	v_lshl_add_u32 v5, v5, 1, s6
	v_cvt_pk_f16_f32 v3, v24, v25
	v_cvt_pk_f16_f32 v2, v22, v23
	v_cvt_pk_f16_f32 v15, v20, v21
	v_lshl_add_u32 v28, v30, 5, v5
	ds_read_b128 v[20:23], v14
	ds_read_b64_tr_b16 v[24:25], v28
	ds_read_b64_tr_b16 v[26:27], v28 offset:512
	v_lshl_add_u32 v5, v29, 5, v5
	v_cvt_pk_f16_f32 v1, v16, v17
	v_cvt_pk_f16_f32 v14, v18, v19
	ds_read_b64_tr_b16 v[16:17], v28 offset:1024
	ds_read_b64_tr_b16 v[18:19], v28 offset:1536
	v_cvt_pk_f16_f32 v28, v6, v7
	ds_read_b64_tr_b16 v[6:7], v5 offset:2048
	s_waitcnt lgkmcnt(3)
	v_mfma_f32_16x16x32_f16 v[0:3], v[24:27], v[0:3], v[20:23]
	v_cvt_pk_f16_f32 v13, v12, v13
	v_cvt_pk_f16_f32 v12, v10, v11
	v_cvt_pk_f16_f32 v5, v8, v9
	v_mov_b32_e32 v8, v4
	v_mov_b32_e32 v9, v4
	s_waitcnt lgkmcnt(1)
	v_mfma_f32_16x16x32_f16 v[10:13], v[16:19], v[12:15], v[0:3]
	s_nop 2
	v_cndmask_b32_e64 v3, v5, 0, vcc
	v_cndmask_b32_e64 v2, v28, 0, vcc
	v_mov_b32_e32 v5, v4
	s_waitcnt lgkmcnt(0)
	s_nop 0
	v_mfma_f32_16x16x32_f16 v[0:3], v[6:9], v[2:5], v[10:13]
	s_and_saveexec_b64 s[6:7], s[2:3]
	s_xor_b64 s[2:3], exec, s[6:7]
	s_cbranch_execz .LBB2_35
	v_cmp_ne_u32_e32 vcc, 3, v50
	s_and_saveexec_b64 s[6:7], vcc
	s_cbranch_execz .LBB2_34
	v_cmp_ne_u32_e32 vcc, 1, v50
	s_and_saveexec_b64 s[8:9], vcc
	s_xor_b64 s[8:9], exec, s[8:9]
	v_lshl_add_u32 v4, v56, 1, v56
	v_mov_b32_e32 v5, 0
	v_lshl_add_u64 v[4:5], v[4:5], 2, s[64:65]
	s_mov_b64 s[10:11], 0x70000
	v_lshl_add_u64 v[4:5], v[4:5], 0, s[10:11]
	s_andn2_saveexec_b64 s[8:9], s[8:9]
	v_mul_u32_u24_e32 v4, 7, v56
	v_mov_b32_e32 v5, 0
	v_lshl_add_u64 v[4:5], v[4:5], 2, s[64:65]
	v_lshl_add_u64 v[4:5], v[4:5], 0, 16
	s_or_b64 exec, exec, s[8:9]
	v_max3_f32 v3, v0, v1, v2
	v_sub_f32_e32 v0, v0, v3
	v_sub_f32_e32 v1, v1, v3
	v_mul_f32_e32 v0, 0x3fb8aa3b, v0
	v_mul_f32_e32 v1, 0x3fb8aa3b, v1
	v_sub_f32_e32 v2, v2, v3
	v_exp_f32_e32 v0, v0
	v_exp_f32_e32 v1, v1
	v_mul_f32_e32 v2, 0x3fb8aa3b, v2
	v_exp_f32_e32 v3, v2
	v_add_f32_e32 v2, v0, v1
	v_add_f32_e32 v2, v3, v2
	v_rcp_f32_e32 v2, v2
	s_nop 0
	v_pk_mul_f32 v[0:1], v[0:1], v[2:3] op_sel_hi:[1,0]
	v_mul_f32_e32 v2, v3, v2
	global_store_dwordx3 v[4:5], v[0:2], off

.LBB2_35:
	s_andn2_saveexec_b64 s[2:3], s[2:3]
	s_cbranch_execz .LBB2_37
	s_nop 2
	v_mul_f32_e32 v0, 0xbfb8aa3b, v0
	v_mul_f32_e32 v1, 0xbfb8aa3b, v1
	v_mul_f32_e32 v2, 0xbfb8aa3b, v2
	v_mul_f32_e32 v3, 0xbfb8aa3b, v3
	v_exp_f32_e32 v0, v0
	v_exp_f32_e32 v1, v1
	v_exp_f32_e32 v2, v2
	v_exp_f32_e32 v3, v3
	v_mul_u32_u24_e32 v4, 7, v56
	v_mov_b32_e32 v5, 0
	v_pk_add_f32 v[0:1], v[0:1], 1.0 op_sel_hi:[1,0]
	v_pk_add_f32 v[2:3], v[2:3], 1.0 op_sel_hi:[1,0]
	v_lshl_add_u64 v[4:5], v[4:5], 2, s[64:65]
	v_rcp_f32_e32 v0, v0
	v_rcp_f32_e32 v1, v1
	v_rcp_f32_e32 v2, v2
	v_rcp_f32_e32 v3, v3
	s_nop 0
	global_store_dwordx4 v[4:5], v[0:3], off
